# v15 + grid barrier hop reduction with the 16 XCD releases issued as one 16-lane atomic (instead of a 16-iteration scalar loop)
# baseline (speedup 1.0000x reference)
; __device__ __forceinline__ unsigned xb_ld(unsigned* p)              { return __hip_atomic_load(p, __ATOMIC_RELAXED, __HIP_MEMORY_SCOPE_AGENT); }
; __device__ __forceinline__ unsigned xb_add(unsigned* p, unsigned v) { return __hip_atomic_fetch_add(p, v, __ATOMIC_RELAXED, __HIP_MEMORY_SCOPE_AGENT); }
; #define XB_SPIN(cond, bar) do { unsigned _sp = 0; while (cond) { __builtin_amdgcn_s_sleep(1); \
;     if ((++_sp & 255u) == 0u) { if (xb_ld(&(bar)[XB_TMO])) break; if (_sp > XB_SPIN_CAP) { atomicAdd(&(bar)[XB_TMO], 1u); break; } } } } while (0)
; __device__ __forceinline__ void xcd_barrier(const XcdBarrier& b) {
;     ...
;             if (og + 1u == (tg + 1u) * nx) xb_add(&bar[XB_TOPGEN], 1u);
;             else XB_SPIN(xb_ld(&bar[XB_TOPGEN]) == tg, bar);
;             __builtin_amdgcn_fence(__ATOMIC_ACQUIRE, "agent");
;             xb_add(&bar[XB_XGEN(b.x)], 1u);
.LBB0_181:
	s_or_b64 exec, exec, s[10:11]
	s_and_saveexec_b64 s[10:11], s[14:15]
	s_cbranch_execz .LBB0_183
	v_mov_b32_e32 v1, 1
	global_atomic_add v[2:3], v1, off
	s_mov_b64 s[12:13], exec
	s_mov_b64 exec, 0xffff
	v_mbcnt_lo_u32_b32 v21, -1, 0
	v_lshlrev_b32_e32 v21, 8, v21
	v_add_u32_e32 v21, 0x2000, v21
	v_mov_b32_e32 v22, 1
	global_atomic_add v21, v22, s[28:29] offset:1024
	s_mov_b64 exec, s[12:13]

; __device__ __forceinline__ unsigned xb_ld(unsigned* p)              { return __hip_atomic_load(p, __ATOMIC_RELAXED, __HIP_MEMORY_SCOPE_AGENT); }
; __device__ __forceinline__ unsigned xb_add(unsigned* p, unsigned v) { return __hip_atomic_fetch_add(p, v, __ATOMIC_RELAXED, __HIP_MEMORY_SCOPE_AGENT); }
; #define XB_SPIN(cond, bar) do { unsigned _sp = 0; while (cond) { __builtin_amdgcn_s_sleep(1); \
;     if ((++_sp & 255u) == 0u) { if (xb_ld(&(bar)[XB_TMO])) break; if (_sp > XB_SPIN_CAP) { atomicAdd(&(bar)[XB_TMO], 1u); break; } } } } while (0)
; __device__ __forceinline__ void xcd_barrier(const XcdBarrier& b) {
;     ...
;             if (og + 1u == (tg + 1u) * nx) xb_add(&bar[XB_TOPGEN], 1u);
;             else XB_SPIN(xb_ld(&bar[XB_TOPGEN]) == tg, bar);
;             __builtin_amdgcn_fence(__ATOMIC_ACQUIRE, "agent");
;             xb_add(&bar[XB_XGEN(b.x)], 1u);
.LBB0_1438:
	s_or_b64 exec, exec, s[8:9]
	s_and_saveexec_b64 s[8:9], s[12:13]
	s_cbranch_execz .LBB0_1440
	v_mov_b32_e32 v1, 1
	global_atomic_add v[2:3], v1, off
	s_mov_b64 s[10:11], exec
	s_mov_b64 exec, 0xffff
	v_mbcnt_lo_u32_b32 v21, -1, 0
	v_lshlrev_b32_e32 v21, 8, v21
	v_add_u32_e32 v21, 0x2000, v21
	v_mov_b32_e32 v22, 1
	global_atomic_add v21, v22, s[28:29] offset:1024
	s_mov_b64 exec, s[10:11]
